# speedup vs baseline: 1.0048x; 1.0007x over previous
.LBB4_49:
	s_or_b64 exec, exec, s[16:17]
	v_mbcnt_hi_u32_b32 v1, -1, v1
	s_waitcnt vmcnt(0)
	v_and_b32_e32 v31, 64, v1
	v_xor_b32_e32 v30, 16, v1
	v_add_u32_e32 v32, 64, v31
	v_cmp_lt_i32_e64 s[0:1], v30, v32
	v_xor_b32_e32 v34, 32, v1
	s_mov_b32 s8, 0
	v_cndmask_b32_e64 v30, v1, v30, s[0:1]
	v_lshlrev_b32_e32 v33, 2, v30
	v_cmp_lt_i32_e64 s[0:1], v34, v32
	ds_bpermute_b32 v30, v33, v46
	ds_bpermute_b32 v31, v33, v47
	v_cndmask_b32_e64 v1, v1, v34, s[0:1]
	ds_bpermute_b32 v34, v33, v48
	ds_bpermute_b32 v35, v33, v49
	v_lshlrev_b32_e32 v1, 2, v1
	s_waitcnt lgkmcnt(2)
	v_add_f32_e32 v30, v46, v30
	v_add_f32_e32 v31, v47, v31
	ds_bpermute_b32 v32, v1, v30
	ds_bpermute_b32 v33, v1, v31
	s_waitcnt lgkmcnt(2)
	v_add_f32_e32 v34, v48, v34
	v_add_f32_e32 v35, v49, v35
	ds_bpermute_b32 v36, v1, v34
	ds_bpermute_b32 v37, v1, v35
	s_and_saveexec_b64 s[4:5], s[2:3]
	s_cbranch_execz .LBB4_51
	v_cvt_f32_i32_e32 v1, v57
	s_mov_b32 s0, 0x800000
	s_waitcnt lgkmcnt(2)
	v_add_f32_e32 v30, v30, v32
	v_add_f32_e32 v31, v31, v33
	s_waitcnt lgkmcnt(0)
	v_add_f32_e32 v32, v34, v36
	v_add_f32_e32 v33, v35, v37
	v_add_f32_e32 v1, 1.0, v1
	v_mul_f32_e32 v46, 0x4b800000, v1
	v_cmp_gt_f32_e64 s[0:1], s0, v1
	v_lshl_or_b32 v0, v43, 8, v0
	s_nop 0
	v_cndmask_b32_e64 v1, v1, v46, s[0:1]
	v_rsq_f32_e32 v1, v1
	s_nop 0
	v_mul_f32_e32 v34, 0x45800000, v1
	v_cndmask_b32_e64 v34, v1, v34, s[0:1]
	v_mul_f32_e32 v32, v34, v32
	v_mul_f32_e32 v33, v34, v33
	v_mul_f32_e32 v30, v34, v30
	v_mul_f32_e32 v31, v34, v31
	ds_write_b128 v0, v[30:33] offset:25600
